# v12
# baseline (speedup 1.0000x reference)
.LBB1_14:
	v_add_u32_e32 v132, s66, v222
	v_add_u32_e32 v133, s66, v223
	ds_read_b128 v[148:151], v132
	ds_read_b128 v[152:155], v133
	v_add_u32_e32 v132, s67, v222
	v_add_u32_e32 v133, s67, v223
	ds_read_b128 v[156:159], v132
	ds_read_b128 v[160:163], v133
	v_add_u32_e32 v132, s68, v222
	v_add_u32_e32 v136, s68, v223
	v_add_u32_e32 v140, s69, v222
	v_add_u32_e32 v144, s69, v223
	v_lshl_add_u64 v[194:195], s[44:45], 0, v[208:209]
	s_add_i32 m0, s43, 0xc000
	ds_read_b128 v[132:135], v132
	ds_read_b128 v[136:139], v136
	ds_read_b128 v[140:143], v140
	ds_read_b128 v[144:147], v144
	ds_read_b128 v[166:169], v226
	ds_read_b128 v[170:173], v226 offset:2048
	ds_read_b128 v[174:177], v227
	ds_read_b128 v[178:181], v227 offset:2048
	ds_read_b128 v[182:185], v226 offset:4096
	ds_read_b128 v[186:189], v226 offset:6144
	ds_read_b128 v[190:193], v227 offset:4096
	ds_read_b128 v[214:217], v227 offset:6144
	global_load_lds_dwordx4 v[194:195], off
	v_lshl_add_u64 v[194:195], s[44:45], 0, v[210:211]
	s_add_i32 m0, s43, 0xe000
	s_nop 0
	global_load_lds_dwordx4 v[194:195], off
	s_waitcnt vmcnt(8)
	s_waitcnt lgkmcnt(0)
	s_barrier
	s_setprio 1
	s_waitcnt lgkmcnt(0)
	v_mfma_f32_16x16x32_f16 v[128:131], v[148:151], v[166:169], v[128:131]
	v_mfma_f32_16x16x32_f16 v[128:131], v[152:155], v[174:177], v[128:131]
	v_mfma_f32_16x16x32_f16 v[120:123], v[160:163], v[174:177], v[120:123]
	v_mfma_f32_16x16x32_f16 v[120:123], v[156:159], v[166:169], v[120:123]
	v_mfma_f32_16x16x32_f16 v[104:107], v[156:159], v[170:173], v[104:107]
	v_mfma_f32_16x16x32_f16 v[104:107], v[160:163], v[178:181], v[104:107]
	v_mfma_f32_16x16x32_f16 v[112:115], v[152:155], v[178:181], v[112:115]
	v_mfma_f32_16x16x32_f16 v[112:115], v[148:151], v[170:173], v[112:115]
	v_mfma_f32_16x16x32_f16 v[96:99], v[148:151], v[182:185], v[96:99]
	v_mfma_f32_16x16x32_f16 v[96:99], v[152:155], v[190:193], v[96:99]
	v_mfma_f32_16x16x32_f16 v[88:91], v[160:163], v[190:193], v[88:91]
	v_mfma_f32_16x16x32_f16 v[88:91], v[156:159], v[182:185], v[88:91]
	v_mfma_f32_16x16x32_f16 v[72:75], v[156:159], v[186:189], v[72:75]
	v_mfma_f32_16x16x32_f16 v[72:75], v[160:163], v[214:217], v[72:75]
	v_mfma_f32_16x16x32_f16 v[80:83], v[152:155], v[214:217], v[80:83]
	v_mfma_f32_16x16x32_f16 v[80:83], v[148:151], v[186:189], v[80:83]
	s_setprio 0
	s_setprio 1
	v_mfma_f32_16x16x32_f16 v[124:127], v[132:135], v[166:169], v[124:127]
	v_mfma_f32_16x16x32_f16 v[124:127], v[136:139], v[174:177], v[124:127]
	v_mfma_f32_16x16x32_f16 v[116:119], v[144:147], v[174:177], v[116:119]
	v_mfma_f32_16x16x32_f16 v[116:119], v[140:143], v[166:169], v[116:119]
	v_mfma_f32_16x16x32_f16 v[100:103], v[140:143], v[170:173], v[100:103]
	v_mfma_f32_16x16x32_f16 v[100:103], v[144:147], v[178:181], v[100:103]
	v_mfma_f32_16x16x32_f16 v[108:111], v[136:139], v[178:181], v[108:111]
	v_mfma_f32_16x16x32_f16 v[108:111], v[132:135], v[170:173], v[108:111]
	v_mfma_f32_16x16x32_f16 v[92:95], v[132:135], v[182:185], v[92:95]
	v_mfma_f32_16x16x32_f16 v[92:95], v[136:139], v[190:193], v[92:95]
	v_mfma_f32_16x16x32_f16 v[84:87], v[144:147], v[190:193], v[84:87]
	v_mfma_f32_16x16x32_f16 v[84:87], v[140:143], v[182:185], v[84:87]
	v_mfma_f32_16x16x32_f16 v[68:71], v[140:143], v[186:189], v[68:71]
	v_mfma_f32_16x16x32_f16 v[68:71], v[144:147], v[214:217], v[68:71]
	v_mfma_f32_16x16x32_f16 v[76:79], v[136:139], v[214:217], v[76:79]
	v_mfma_f32_16x16x32_f16 v[76:79], v[132:135], v[186:189], v[76:79]
	s_setprio 0
	s_barrier
	s_andn2_b64 vcc, exec, s[4:5]
	s_cbranch_vccnz .LBB1_16
	v_cvt_pkrtz_f16_f32 v166, v0, v1
	v_cvt_pkrtz_f16_f32 v167, v2, v3
	v_add_u32_e32 v166, 0x20002, v166
	v_add_u32_e32 v167, 0x20002, v167
	v_and_b32_e32 v166, 0xfffcfffc, v166
	v_and_b32_e32 v167, 0xfffcfffc, v167
	global_store_dwordx2 v[164:165], v[166:167], off

.LBB1_20:
	s_waitcnt lgkmcnt(0)
	s_barrier
	s_setprio 1
	s_waitcnt lgkmcnt(0)
	v_mfma_f32_16x16x32_f16 v[64:67], v[148:151], v[188:191], v[64:67]
	v_mfma_f32_16x16x32_f16 v[64:67], v[152:155], v[192:195], v[64:67]
	v_mfma_f32_16x16x32_f16 v[56:59], v[160:163], v[192:195], v[56:59]
	v_mfma_f32_16x16x32_f16 v[56:59], v[156:159], v[188:191], v[56:59]
	v_mfma_f32_16x16x32_f16 v[40:43], v[156:159], v[176:179], v[40:43]
	v_mfma_f32_16x16x32_f16 v[40:43], v[160:163], v[180:183], v[40:43]
	v_mfma_f32_16x16x32_f16 v[48:51], v[152:155], v[180:183], v[48:51]
	v_mfma_f32_16x16x32_f16 v[48:51], v[148:151], v[176:179], v[48:51]
	v_mfma_f32_16x16x32_f16 v[32:35], v[148:151], v[172:175], v[32:35]
	v_mfma_f32_16x16x32_f16 v[32:35], v[152:155], v[184:187], v[32:35]
	v_mfma_f32_16x16x32_f16 v[24:27], v[160:163], v[184:187], v[24:27]
	v_mfma_f32_16x16x32_f16 v[24:27], v[156:159], v[172:175], v[24:27]
	v_mfma_f32_16x16x32_f16 v[8:11], v[156:159], v[164:167], v[8:11]
	v_mfma_f32_16x16x32_f16 v[8:11], v[160:163], v[168:171], v[8:11]
	v_mfma_f32_16x16x32_f16 v[16:19], v[152:155], v[168:171], v[16:19]
	v_mfma_f32_16x16x32_f16 v[16:19], v[148:151], v[164:167], v[16:19]
	s_setprio 0
	s_setprio 1
	v_mfma_f32_16x16x32_f16 v[60:63], v[132:135], v[188:191], v[60:63]
	v_mfma_f32_16x16x32_f16 v[60:63], v[136:139], v[192:195], v[60:63]
	v_mfma_f32_16x16x32_f16 v[52:55], v[144:147], v[192:195], v[52:55]
	v_mfma_f32_16x16x32_f16 v[52:55], v[140:143], v[188:191], v[52:55]
	v_mfma_f32_16x16x32_f16 v[36:39], v[140:143], v[176:179], v[36:39]
	v_mfma_f32_16x16x32_f16 v[36:39], v[144:147], v[180:183], v[36:39]
	v_mfma_f32_16x16x32_f16 v[44:47], v[136:139], v[180:183], v[44:47]
	v_mfma_f32_16x16x32_f16 v[44:47], v[132:135], v[176:179], v[44:47]
	v_mfma_f32_16x16x32_f16 v[28:31], v[132:135], v[172:175], v[28:31]
	v_mfma_f32_16x16x32_f16 v[28:31], v[136:139], v[184:187], v[28:31]
	v_mfma_f32_16x16x32_f16 v[20:23], v[144:147], v[184:187], v[20:23]
	v_mfma_f32_16x16x32_f16 v[20:23], v[140:143], v[172:175], v[20:23]
	v_mfma_f32_16x16x32_f16 v[4:7], v[140:143], v[164:167], v[4:7]
	v_mfma_f32_16x16x32_f16 v[4:7], v[144:147], v[168:171], v[4:7]
	v_mfma_f32_16x16x32_f16 v[12:15], v[136:139], v[168:171], v[12:15]
	v_mfma_f32_16x16x32_f16 v[12:15], v[132:135], v[164:167], v[12:15]
	s_setprio 0
	s_barrier
	v_add_u32_e32 v132, s70, v222
	s_add_u32 s48, s48, 0x100000
	v_add_u32_e32 v133, s70, v223
	ds_read_b128 v[148:151], v132
	ds_read_b128 v[152:155], v133
	v_add_u32_e32 v132, s71, v222
	s_addc_u32 s49, s49, 0
	s_mov_b32 m0, s57
	v_add_u32_e32 v133, s71, v223
	ds_read_b128 v[156:159], v132
	ds_read_b128 v[160:163], v133
	v_add_u32_e32 v132, s72, v222
	v_add_u32_e32 v136, s72, v223
	v_add_u32_e32 v140, s73, v222
	v_add_u32_e32 v144, s73, v223
	v_lshl_add_u64 v[212:213], s[48:49], 0, v[202:203]
	ds_read_b128 v[132:135], v132
	ds_read_b128 v[136:139], v136
	ds_read_b128 v[140:143], v140
	ds_read_b128 v[144:147], v144
	ds_read_b128 v[188:191], v226 offset:32768
	ds_read_b128 v[176:179], v226 offset:34816
	ds_read_b128 v[192:195], v227 offset:32768
	ds_read_b128 v[180:183], v227 offset:34816
	ds_read_b128 v[172:175], v226 offset:36864
	ds_read_b128 v[164:167], v226 offset:38912
	ds_read_b128 v[184:187], v227 offset:36864
	ds_read_b128 v[168:171], v227 offset:38912
	global_load_lds_dwordx4 v[212:213], off
	v_lshl_add_u64 v[212:213], s[48:49], 0, v[198:199]
	s_mov_b32 m0, s58
	s_mov_b64 s[48:49], -1
	global_load_lds_dwordx4 v[212:213], off
	s_mov_b64 vcc, s[4:5]
	s_cbranch_vccz .LBB1_22
	s_waitcnt vmcnt(8)
	s_mov_b64 s[48:49], 0

.LBB1_24:
	s_waitcnt lgkmcnt(0)
	s_barrier
	s_setprio 1
	s_waitcnt lgkmcnt(0)
	v_mfma_f32_16x16x32_f16 v[128:131], v[148:151], v[188:191], v[128:131]
	v_mfma_f32_16x16x32_f16 v[128:131], v[152:155], v[192:195], v[128:131]
	v_mfma_f32_16x16x32_f16 v[120:123], v[160:163], v[192:195], v[120:123]
	v_mfma_f32_16x16x32_f16 v[120:123], v[156:159], v[188:191], v[120:123]
	v_mfma_f32_16x16x32_f16 v[104:107], v[156:159], v[176:179], v[104:107]
	v_mfma_f32_16x16x32_f16 v[104:107], v[160:163], v[180:183], v[104:107]
	v_mfma_f32_16x16x32_f16 v[112:115], v[152:155], v[180:183], v[112:115]
	v_mfma_f32_16x16x32_f16 v[112:115], v[148:151], v[176:179], v[112:115]
	v_mfma_f32_16x16x32_f16 v[96:99], v[148:151], v[172:175], v[96:99]
	v_mfma_f32_16x16x32_f16 v[96:99], v[152:155], v[184:187], v[96:99]
	v_mfma_f32_16x16x32_f16 v[88:91], v[160:163], v[184:187], v[88:91]
	v_mfma_f32_16x16x32_f16 v[88:91], v[156:159], v[172:175], v[88:91]
	v_mfma_f32_16x16x32_f16 v[72:75], v[156:159], v[164:167], v[72:75]
	v_mfma_f32_16x16x32_f16 v[72:75], v[160:163], v[168:171], v[72:75]
	v_mfma_f32_16x16x32_f16 v[80:83], v[152:155], v[168:171], v[80:83]
	v_mfma_f32_16x16x32_f16 v[80:83], v[148:151], v[164:167], v[80:83]
	s_setprio 0
	s_setprio 1
	v_mfma_f32_16x16x32_f16 v[124:127], v[132:135], v[188:191], v[124:127]
	v_mfma_f32_16x16x32_f16 v[124:127], v[136:139], v[192:195], v[124:127]
	v_mfma_f32_16x16x32_f16 v[116:119], v[144:147], v[192:195], v[116:119]
	v_mfma_f32_16x16x32_f16 v[116:119], v[140:143], v[188:191], v[116:119]
	v_mfma_f32_16x16x32_f16 v[100:103], v[140:143], v[176:179], v[100:103]
	v_mfma_f32_16x16x32_f16 v[100:103], v[144:147], v[180:183], v[100:103]
	v_mfma_f32_16x16x32_f16 v[108:111], v[136:139], v[180:183], v[108:111]
	v_mfma_f32_16x16x32_f16 v[108:111], v[132:135], v[176:179], v[108:111]
	v_mfma_f32_16x16x32_f16 v[92:95], v[132:135], v[172:175], v[92:95]
	v_mfma_f32_16x16x32_f16 v[92:95], v[136:139], v[184:187], v[92:95]
	v_mfma_f32_16x16x32_f16 v[84:87], v[144:147], v[184:187], v[84:87]
	v_mfma_f32_16x16x32_f16 v[84:87], v[140:143], v[172:175], v[84:87]
	v_mfma_f32_16x16x32_f16 v[68:71], v[140:143], v[164:167], v[68:71]
	v_mfma_f32_16x16x32_f16 v[68:71], v[144:147], v[168:171], v[68:71]
	v_mfma_f32_16x16x32_f16 v[76:79], v[136:139], v[168:171], v[76:79]
	v_mfma_f32_16x16x32_f16 v[76:79], v[132:135], v[164:167], v[76:79]
	s_setprio 0
	s_barrier
	s_mov_b32 m0, s59
	v_lshl_add_u64 v[212:213], v[214:215], 0, s[24:25]
	s_add_u32 s4, s46, 0x100080
	ds_read_b128 v[164:167], v226 offset:49152
	ds_read_b128 v[168:171], v226 offset:51200
	ds_read_b128 v[172:175], v227 offset:49152
	ds_read_b128 v[176:179], v227 offset:51200
	ds_read_b128 v[180:183], v226 offset:53248
	ds_read_b128 v[184:187], v226 offset:55296
	ds_read_b128 v[188:191], v227 offset:53248
	ds_read_b128 v[192:195], v227 offset:55296
	global_load_lds_dwordx4 v[212:213], off
	v_lshl_add_u64 v[212:213], v[216:217], 0, s[24:25]
	s_mov_b32 m0, s60
	s_addc_u32 s5, s47, 0
	global_load_lds_dwordx4 v[212:213], off
	v_lshl_add_u64 v[212:213], s[4:5], 0, v[200:201]
	s_mov_b32 m0, s63
	s_nop 0
	global_load_lds_dwordx4 v[212:213], off
	v_lshl_add_u64 v[212:213], s[4:5], 0, v[196:197]
	s_mov_b32 m0, s64
	s_nop 0
	global_load_lds_dwordx4 v[212:213], off
	v_lshl_add_u64 v[212:213], v[218:219], 0, s[24:25]
	s_mov_b32 m0, s61
	s_nop 0
	global_load_lds_dwordx4 v[212:213], off
	v_lshl_add_u64 v[212:213], v[220:221], 0, s[24:25]
	s_mov_b32 m0, s62
	s_nop 0
	global_load_lds_dwordx4 v[212:213], off
	s_waitcnt vmcnt(8)
	s_waitcnt lgkmcnt(0)
	s_barrier
	s_setprio 1
	s_waitcnt lgkmcnt(0)
	v_mfma_f32_16x16x32_f16 v[64:67], v[148:151], v[164:167], v[64:67]
	v_mfma_f32_16x16x32_f16 v[64:67], v[152:155], v[172:175], v[64:67]
	v_mfma_f32_16x16x32_f16 v[56:59], v[160:163], v[172:175], v[56:59]
	v_mfma_f32_16x16x32_f16 v[56:59], v[156:159], v[164:167], v[56:59]
	v_mfma_f32_16x16x32_f16 v[40:43], v[156:159], v[168:171], v[40:43]
	v_mfma_f32_16x16x32_f16 v[40:43], v[160:163], v[176:179], v[40:43]
	v_mfma_f32_16x16x32_f16 v[48:51], v[152:155], v[176:179], v[48:51]
	v_mfma_f32_16x16x32_f16 v[48:51], v[148:151], v[168:171], v[48:51]
	v_mfma_f32_16x16x32_f16 v[32:35], v[148:151], v[180:183], v[32:35]
	v_mfma_f32_16x16x32_f16 v[32:35], v[152:155], v[188:191], v[32:35]
	v_mfma_f32_16x16x32_f16 v[24:27], v[160:163], v[188:191], v[24:27]
	v_mfma_f32_16x16x32_f16 v[24:27], v[156:159], v[180:183], v[24:27]
	v_mfma_f32_16x16x32_f16 v[8:11], v[156:159], v[184:187], v[8:11]
	v_mfma_f32_16x16x32_f16 v[8:11], v[160:163], v[192:195], v[8:11]
	v_mfma_f32_16x16x32_f16 v[16:19], v[152:155], v[192:195], v[16:19]
	v_mfma_f32_16x16x32_f16 v[16:19], v[148:151], v[184:187], v[16:19]
	s_setprio 0
	s_setprio 1
	v_mfma_f32_16x16x32_f16 v[60:63], v[132:135], v[164:167], v[60:63]
	v_mfma_f32_16x16x32_f16 v[60:63], v[136:139], v[172:175], v[60:63]
	v_mfma_f32_16x16x32_f16 v[52:55], v[144:147], v[172:175], v[52:55]
	v_mfma_f32_16x16x32_f16 v[52:55], v[140:143], v[164:167], v[52:55]
	v_mfma_f32_16x16x32_f16 v[36:39], v[140:143], v[168:171], v[36:39]
	v_mfma_f32_16x16x32_f16 v[36:39], v[144:147], v[176:179], v[36:39]
	v_mfma_f32_16x16x32_f16 v[44:47], v[136:139], v[176:179], v[44:47]
	v_mfma_f32_16x16x32_f16 v[44:47], v[132:135], v[168:171], v[44:47]
	v_mfma_f32_16x16x32_f16 v[28:31], v[132:135], v[180:183], v[28:31]
	v_mfma_f32_16x16x32_f16 v[28:31], v[136:139], v[188:191], v[28:31]
	v_mfma_f32_16x16x32_f16 v[20:23], v[144:147], v[188:191], v[20:23]
	v_mfma_f32_16x16x32_f16 v[20:23], v[140:143], v[180:183], v[20:23]
	v_mfma_f32_16x16x32_f16 v[4:7], v[140:143], v[184:187], v[4:7]
	v_mfma_f32_16x16x32_f16 v[4:7], v[144:147], v[192:195], v[4:7]
	v_mfma_f32_16x16x32_f16 v[12:15], v[136:139], v[192:195], v[12:15]
	v_mfma_f32_16x16x32_f16 v[12:15], v[132:135], v[184:187], v[12:15]
	s_setprio 0
	s_barrier
	s_add_u32 s80, s80, 0x100
	s_addc_u32 s81, s81, 0
	s_add_u32 s44, s44, 0x100
	s_addc_u32 s45, s45, 0
	s_cmp_gt_u32 s82, 61
	s_cbranch_scc1 .LBB1_4
	s_mov_b32 s48, s82
	s_branch .LBB1_9

.LBB2_5:
	s_add_i32 s8, s10, s8
	s_ashr_i32 s9, s8, 31
	s_lshr_b32 s9, s9, 25
	s_add_i32 s9, s8, s9
	s_ashr_i32 s10, s9, 7
	s_and_b32 s9, s9, 0xff80
	s_sub_i32 s8, s8, s9
	s_bfe_i32 s9, s8, 0x80000
	s_bfe_u32 s9, s9, 0x3000c
	s_add_i32 s9, s8, s9
	s_bfe_i32 s11, s9, 0x80000
	s_and_b32 s9, s9, 0xf8
	s_sub_i32 s8, s8, s9
	v_lshrrev_b32_e32 v2, 3, v0
	s_lshl_b32 s10, s10, 3
	s_sext_i32_i16 s11, s11
	s_sext_i32_i8 s8, s8
	v_xor_b32_e32 v1, v2, v0
	s_lshr_b32 s17, s33, 6
	s_add_i32 s55, s10, s8
	s_ashr_i32 s10, s11, 3
	s_lshr_b32 s16, s33, 8
	v_lshlrev_b32_e32 v3, 3, v1
	s_lshl_b32 s36, s17, 10
	s_lshr_b32 s18, s11, 3
	s_mul_hi_i32 s11, s10, 0x700000
	s_mul_i32 s10, s10, 0x700000
	v_and_b32_e32 v3, 56, v3
	v_mul_u32_u24_e32 v2, 0x3800, v2
	s_waitcnt lgkmcnt(0)
	s_add_u32 s28, s6, s10
	v_or_b32_e32 v4, v2, v3
	s_addc_u32 s29, s7, s11
	s_add_i32 s37, s36, 0
	v_lshlrev_b32_e32 v128, 1, v4
	s_add_i32 m0, s37, 0x10000
	s_mul_i32 s9, s55, 0x700000
	global_load_lds_dwordx4 v128, s[28:29]
	s_add_i32 m0, s37, 0x12000
	v_add_u32_e32 v130, 0x1c0000, v128
	s_mul_hi_i32 s8, s55, 0x700000
	s_add_u32 s30, s4, s9
	global_load_lds_dwordx4 v130, s[28:29]
	s_addc_u32 s31, s5, s8
	s_mov_b32 m0, s37
	s_add_i32 s38, s37, 0x2000
	global_load_lds_dwordx4 v128, s[30:31]
	s_mov_b32 m0, s38
	s_add_u32 s8, s28, 0x380000
	global_load_lds_dwordx4 v130, s[30:31]
	s_addc_u32 s9, s29, 0
	s_add_i32 m0, s37, 0x14000
	v_mov_b32_e32 v129, 0
	global_load_lds_dwordx4 v128, s[8:9]
	s_add_i32 m0, s37, 0x16000
	v_lshl_add_u64 v[4:5], s[28:29], 0, v[128:129]
	global_load_lds_dwordx4 v130, s[8:9]
	s_add_u32 s8, s30, 0x380000
	s_addc_u32 s9, s31, 0
	s_add_i32 s39, s37, 0x4000
	s_mov_b32 m0, s39
	s_add_i32 s40, s37, 0x6000
	v_mov_b32_e32 v131, v129
	global_load_lds_dwordx4 v128, s[8:9]
	s_mov_b32 m0, s40
	s_mov_b64 s[14:15], 0x80
	v_lshl_add_u64 v[6:7], s[28:29], 0, v[130:131]
	global_load_lds_dwordx4 v130, s[8:9]
	s_add_i32 m0, s37, 0x18000
	v_lshl_add_u64 v[4:5], v[4:5], 0, s[14:15]
	v_lshl_add_u64 v[8:9], s[30:31], 0, v[128:129]
	global_load_lds_dwordx4 v[4:5], off
	v_lshl_add_u64 v[4:5], v[6:7], 0, s[14:15]
	s_add_i32 m0, s37, 0x1a000
	s_add_i32 s41, s37, 0x8000
	v_lshl_add_u64 v[10:11], s[30:31], 0, v[130:131]
	global_load_lds_dwordx4 v[4:5], off
	v_lshl_add_u64 v[4:5], v[8:9], 0, s[14:15]
	s_mov_b32 m0, s41
	s_add_i32 s42, s37, 0xa000
	global_load_lds_dwordx4 v[4:5], off
	v_lshl_add_u64 v[4:5], v[10:11], 0, s[14:15]
	s_mov_b32 m0, s42
	s_add_u32 s8, s28, 0x380080
	global_load_lds_dwordx4 v[4:5], off
	s_addc_u32 s9, s29, 0
	s_add_i32 m0, s37, 0x1c000
	s_mov_b32 s45, 0
	global_load_lds_dwordx4 v128, s[8:9]
	s_add_i32 m0, s37, 0x1e000
	s_cmp_lg_u32 s16, 1
	global_load_lds_dwordx4 v130, s[8:9]
	s_load_dwordx4 s[8:11], s[0:1], 0x10
	s_waitcnt vmcnt(6)
	s_barrier
	s_cbranch_scc1 .LBB2_7
	s_barrier
.LBB2_7:
	s_lshl_b32 s0, s17, 5
	v_lshrrev_b32_e32 v4, 4, v0
	v_and_b32_e32 v5, 15, v0
	v_bfe_u32 v6, v0, 4, 2
	v_and_b32_e32 v0, 7, v0
	s_and_b32 s0, s0, 0x60
	v_lshl_or_b32 v137, s16, 6, v5
	v_bitop3_b32 v4, v4, v0, 3 bitop3:0x6c
	v_bitop3_b32 v0, v6, v0, 4 bitop3:0x36
	v_or_b32_e32 v5, s0, v5
	v_lshlrev_b32_e32 v7, 7, v137
	v_lshlrev_b32_e32 v4, 4, v4
	v_lshlrev_b32_e32 v0, 4, v0
	v_lshlrev_b32_e32 v5, 7, v5
	v_or_b32_e32 v8, v7, v4
	v_or_b32_e32 v7, v7, v0
	v_or_b32_e32 v4, v5, v4
	v_or_b32_e32 v0, v5, v0
	v_lshl_or_b32 v141, v6, 2, s0
	s_add_i32 s0, 0, 0x10800
	v_add_u32_e32 v149, s0, v4
	v_add_u32_e32 v150, s0, v0
	s_add_i32 s0, 0, 0x14800
	v_add_u32_e32 v153, s0, v4
	v_add_u32_e32 v154, s0, v0
	s_add_i32 s0, 0, 0x18800
	v_add_u32_e32 v3, v2, v3
	v_mov_b32_e32 v5, 0x1c0000
	v_and_b32_e32 v1, 7, v1
	v_lshlrev_b32_e32 v2, 1, v2
	s_add_i32 s43, 0, 0x10000
	s_add_i32 s44, 0, 0x14000
	s_add_i32 s46, 0, 0x18000
	v_add_u32_e32 v159, s0, v4
	v_add_u32_e32 v160, s0, v0
	s_add_i32 s47, 0, 0x1c000
	s_add_i32 s0, 0, 0x1c800
	s_sext_i32_i8 s54, s18
	v_lshl_add_u32 v132, v3, 1, v5
	v_mov_b32_e32 v133, v129
	v_lshl_add_u32 v134, v1, 4, v2
	v_mov_b32_e32 v135, v129
	v_add_u32_e32 v143, s43, v4
	v_add_u32_e32 v147, s43, v0
	v_add_u32_e32 v151, s44, v4
	v_add_u32_e32 v152, s44, v0
	v_add_u32_e32 v155, 0, v8
	v_add_u32_e32 v156, 0, v7
	v_add_u32_e32 v157, s46, v4
	v_add_u32_e32 v158, s46, v0
	v_add_u32_e32 v161, s47, v4
	v_add_u32_e32 v162, s47, v0
	v_add_u32_e32 v163, s0, v4
	v_add_u32_e32 v164, s0, v0
	s_mov_b64 s[16:17], 0x200000
	s_mov_b32 s48, 0x200000
	s_mov_b64 s[18:19], 0x240000
	s_mov_b32 s49, 0x240000
	s_mov_b64 s[20:21], 0x280000
	s_mov_b32 s50, 0x280000
	s_mov_b64 s[22:23], 0x2c0000
	s_mov_b32 s51, 0x2c0000
	s_mov_b32 s53, 0
	s_mov_b32 s52, 0

.LBB2_20:
	s_add_u32 s30, s28, 0xffc80080
	s_addc_u32 s31, s29, -1
	s_cmpk_eq_i32 s58, 0xdc
	s_cselect_b32 s35, s25, s31
	s_cselect_b32 s34, s24, s30
	s_cselect_b32 s31, s27, s57
	s_cselect_b32 s30, s26, s56
	v_lshl_add_u64 v[138:139], s[28:29], 0, v[134:135]
	s_add_i32 m0, s37, 0xc000
	ds_read_b128 v[166:169], v143
	ds_read_b128 v[170:173], v147
	ds_read_b128 v[174:177], v149
	ds_read_b128 v[178:181], v150
	ds_read_b128 v[182:185], v151
	ds_read_b128 v[186:189], v152
	ds_read_b128 v[190:193], v153
	ds_read_b128 v[194:197], v154
	ds_read_b128 v[198:201], v155
	ds_read_b128 v[202:205], v155 offset:2048
	ds_read_b128 v[206:209], v156
	ds_read_b128 v[210:213], v156 offset:2048
	ds_read_b128 v[214:217], v155 offset:4096
	ds_read_b128 v[218:221], v155 offset:6144
	ds_read_b128 v[222:225], v156 offset:4096
	ds_read_b128 v[226:229], v156 offset:6144
	global_load_lds_dwordx4 v[138:139], off
	v_lshl_add_u64 v[138:139], s[28:29], 0, v[132:133]
	s_add_i32 m0, s37, 0xe000
	s_nop 0
	global_load_lds_dwordx4 v[138:139], off
	s_waitcnt vmcnt(8)
	s_waitcnt lgkmcnt(0)
	s_barrier
	s_setprio 1
	s_waitcnt lgkmcnt(0)
	v_mfma_f32_16x16x32_f16 v[124:127], v[166:169], v[198:201], v[124:127]
	v_mfma_f32_16x16x32_f16 v[124:127], v[170:173], v[206:209], v[124:127]
	v_mfma_f32_16x16x32_f16 v[120:123], v[178:181], v[206:209], v[120:123]
	v_mfma_f32_16x16x32_f16 v[120:123], v[174:177], v[198:201], v[120:123]
	v_mfma_f32_16x16x32_f16 v[112:115], v[174:177], v[202:205], v[112:115]
	v_mfma_f32_16x16x32_f16 v[112:115], v[178:181], v[210:213], v[112:115]
	v_mfma_f32_16x16x32_f16 v[116:119], v[170:173], v[210:213], v[116:119]
	v_mfma_f32_16x16x32_f16 v[116:119], v[166:169], v[202:205], v[116:119]
	v_mfma_f32_16x16x32_f16 v[108:111], v[166:169], v[214:217], v[108:111]
	v_mfma_f32_16x16x32_f16 v[108:111], v[170:173], v[222:225], v[108:111]
	v_mfma_f32_16x16x32_f16 v[100:103], v[178:181], v[222:225], v[100:103]
	v_mfma_f32_16x16x32_f16 v[100:103], v[174:177], v[214:217], v[100:103]
	v_mfma_f32_16x16x32_f16 v[84:87], v[174:177], v[218:221], v[84:87]
	v_mfma_f32_16x16x32_f16 v[84:87], v[178:181], v[226:229], v[84:87]
	v_mfma_f32_16x16x32_f16 v[92:95], v[170:173], v[226:229], v[92:95]
	v_mfma_f32_16x16x32_f16 v[92:95], v[166:169], v[218:221], v[92:95]
	s_setprio 0
	s_setprio 1
	v_mfma_f32_16x16x32_f16 v[104:107], v[182:185], v[198:201], v[104:107]
	v_mfma_f32_16x16x32_f16 v[104:107], v[186:189], v[206:209], v[104:107]
	v_mfma_f32_16x16x32_f16 v[96:99], v[194:197], v[206:209], v[96:99]
	v_mfma_f32_16x16x32_f16 v[96:99], v[190:193], v[198:201], v[96:99]
	v_mfma_f32_16x16x32_f16 v[80:83], v[190:193], v[202:205], v[80:83]
	v_mfma_f32_16x16x32_f16 v[80:83], v[194:197], v[210:213], v[80:83]
	v_mfma_f32_16x16x32_f16 v[88:91], v[186:189], v[210:213], v[88:91]
	v_mfma_f32_16x16x32_f16 v[88:91], v[182:185], v[202:205], v[88:91]
	v_mfma_f32_16x16x32_f16 v[76:79], v[182:185], v[214:217], v[76:79]
	v_mfma_f32_16x16x32_f16 v[76:79], v[186:189], v[222:225], v[76:79]
	v_mfma_f32_16x16x32_f16 v[72:75], v[194:197], v[222:225], v[72:75]
	v_mfma_f32_16x16x32_f16 v[72:75], v[190:193], v[214:217], v[72:75]
	v_mfma_f32_16x16x32_f16 v[64:67], v[190:193], v[218:221], v[64:67]
	v_mfma_f32_16x16x32_f16 v[64:67], v[194:197], v[226:229], v[64:67]
	v_mfma_f32_16x16x32_f16 v[68:71], v[186:189], v[226:229], v[68:71]
	v_mfma_f32_16x16x32_f16 v[68:71], v[182:185], v[218:221], v[68:71]
	s_setprio 0
	s_barrier
	s_add_i32 s59, s43, s36
	v_lshl_add_u64 v[138:139], s[30:31], 0, v[128:129]
	s_mov_b32 m0, s59
	ds_read_b128 v[198:201], v155 offset:16384
	ds_read_b128 v[202:205], v155 offset:18432
	ds_read_b128 v[206:209], v156 offset:16384
	ds_read_b128 v[210:213], v156 offset:18432
	ds_read_b128 v[214:217], v155 offset:20480
	ds_read_b128 v[218:221], v155 offset:22528
	ds_read_b128 v[222:225], v156 offset:20480
	ds_read_b128 v[226:229], v156 offset:22528
	global_load_lds_dwordx4 v[138:139], off
	s_add_i32 m0, s59, 0x2000
	s_add_u32 s60, s30, 0x380000
	v_lshl_add_u64 v[144:145], s[30:31], 0, v[130:131]
	s_addc_u32 s61, s31, 0
	s_add_i32 s59, s44, s36
	global_load_lds_dwordx4 v[144:145], off
	v_lshl_add_u64 v[230:231], s[60:61], 0, v[128:129]
	s_mov_b32 m0, s59
	v_lshl_add_u64 v[232:233], s[34:35], 0, v[130:131]
	global_load_lds_dwordx4 v[230:231], off
	v_lshl_add_u64 v[230:231], s[60:61], 0, v[130:131]
	s_add_i32 m0, s59, 0x2000
	s_nop 0
	global_load_lds_dwordx4 v[230:231], off
	v_lshl_add_u64 v[230:231], s[34:35], 0, v[128:129]
	s_mov_b32 m0, s37
	s_nop 0
	global_load_lds_dwordx4 v[230:231], off
	s_mov_b32 m0, s38
	s_nop 0
	global_load_lds_dwordx4 v[232:233], off
	s_waitcnt vmcnt(8)
	s_waitcnt lgkmcnt(0)
	s_barrier
	s_setprio 1
	s_waitcnt lgkmcnt(0)
	v_mfma_f32_16x16x32_f16 v[60:63], v[166:169], v[198:201], v[60:63]
	v_mfma_f32_16x16x32_f16 v[60:63], v[170:173], v[206:209], v[60:63]
	v_mfma_f32_16x16x32_f16 v[56:59], v[178:181], v[206:209], v[56:59]
	v_mfma_f32_16x16x32_f16 v[56:59], v[174:177], v[198:201], v[56:59]
	v_mfma_f32_16x16x32_f16 v[48:51], v[174:177], v[202:205], v[48:51]
	v_mfma_f32_16x16x32_f16 v[48:51], v[178:181], v[210:213], v[48:51]
	v_mfma_f32_16x16x32_f16 v[52:55], v[170:173], v[210:213], v[52:55]
	v_mfma_f32_16x16x32_f16 v[52:55], v[166:169], v[202:205], v[52:55]
	v_mfma_f32_16x16x32_f16 v[40:43], v[166:169], v[214:217], v[40:43]
	v_mfma_f32_16x16x32_f16 v[40:43], v[170:173], v[222:225], v[40:43]
	v_mfma_f32_16x16x32_f16 v[32:35], v[178:181], v[222:225], v[32:35]
	v_mfma_f32_16x16x32_f16 v[32:35], v[174:177], v[214:217], v[32:35]
	v_mfma_f32_16x16x32_f16 v[8:11], v[174:177], v[218:221], v[8:11]
	v_mfma_f32_16x16x32_f16 v[8:11], v[178:181], v[226:229], v[8:11]
	v_mfma_f32_16x16x32_f16 v[12:15], v[170:173], v[226:229], v[12:15]
	v_mfma_f32_16x16x32_f16 v[12:15], v[166:169], v[218:221], v[12:15]
	s_setprio 0
	s_setprio 1
	v_mfma_f32_16x16x32_f16 v[44:47], v[182:185], v[198:201], v[44:47]
	v_mfma_f32_16x16x32_f16 v[44:47], v[186:189], v[206:209], v[44:47]
	v_mfma_f32_16x16x32_f16 v[36:39], v[194:197], v[206:209], v[36:39]
	v_mfma_f32_16x16x32_f16 v[36:39], v[190:193], v[198:201], v[36:39]
	v_mfma_f32_16x16x32_f16 v[24:27], v[190:193], v[202:205], v[24:27]
	v_mfma_f32_16x16x32_f16 v[24:27], v[194:197], v[210:213], v[24:27]
	v_mfma_f32_16x16x32_f16 v[28:31], v[186:189], v[210:213], v[28:31]
	v_mfma_f32_16x16x32_f16 v[28:31], v[182:185], v[202:205], v[28:31]
	v_mfma_f32_16x16x32_f16 v[20:23], v[182:185], v[214:217], v[20:23]
	v_mfma_f32_16x16x32_f16 v[20:23], v[186:189], v[222:225], v[20:23]
	v_mfma_f32_16x16x32_f16 v[16:19], v[194:197], v[222:225], v[16:19]
	v_mfma_f32_16x16x32_f16 v[16:19], v[190:193], v[214:217], v[16:19]
	v_mfma_f32_16x16x32_f16 v[0:3], v[190:193], v[218:221], v[0:3]
	v_mfma_f32_16x16x32_f16 v[0:3], v[194:197], v[226:229], v[0:3]
	v_mfma_f32_16x16x32_f16 v[4:7], v[186:189], v[226:229], v[4:7]
	v_mfma_f32_16x16x32_f16 v[4:7], v[182:185], v[218:221], v[4:7]
	s_setprio 0
	s_barrier
	s_add_u32 s34, s34, 0x380000
	s_addc_u32 s35, s35, 0
	s_mov_b32 m0, s39
	v_lshl_add_u64 v[234:235], s[34:35], 0, v[128:129]
	ds_read_b128 v[166:169], v157
	ds_read_b128 v[170:173], v158
	ds_read_b128 v[174:177], v159
	ds_read_b128 v[178:181], v160
	ds_read_b128 v[182:185], v161
	ds_read_b128 v[186:189], v162
	ds_read_b128 v[190:193], v163
	ds_read_b128 v[194:197], v164
	ds_read_b128 v[198:201], v155 offset:32768
	ds_read_b128 v[202:205], v155 offset:34816
	ds_read_b128 v[206:209], v156 offset:32768
	ds_read_b128 v[210:213], v156 offset:34816
	ds_read_b128 v[214:217], v155 offset:36864
	ds_read_b128 v[218:221], v155 offset:38912
	ds_read_b128 v[222:225], v156 offset:36864
	ds_read_b128 v[226:229], v156 offset:38912
	global_load_lds_dwordx4 v[234:235], off
	v_lshl_add_u64 v[234:235], s[34:35], 0, v[130:131]
	s_mov_b32 m0, s40
	s_nop 0
	global_load_lds_dwordx4 v[234:235], off
	s_waitcnt vmcnt(8)
	s_waitcnt lgkmcnt(0)
	s_barrier
	s_setprio 1
	s_waitcnt lgkmcnt(0)
	v_mfma_f32_16x16x32_f16 v[124:127], v[166:169], v[198:201], v[124:127]
	v_mfma_f32_16x16x32_f16 v[124:127], v[170:173], v[206:209], v[124:127]
	v_mfma_f32_16x16x32_f16 v[120:123], v[178:181], v[206:209], v[120:123]
	v_mfma_f32_16x16x32_f16 v[120:123], v[174:177], v[198:201], v[120:123]
	v_mfma_f32_16x16x32_f16 v[112:115], v[174:177], v[202:205], v[112:115]
	v_mfma_f32_16x16x32_f16 v[112:115], v[178:181], v[210:213], v[112:115]
	v_mfma_f32_16x16x32_f16 v[116:119], v[170:173], v[210:213], v[116:119]
	v_mfma_f32_16x16x32_f16 v[116:119], v[166:169], v[202:205], v[116:119]
	v_mfma_f32_16x16x32_f16 v[108:111], v[166:169], v[214:217], v[108:111]
	v_mfma_f32_16x16x32_f16 v[108:111], v[170:173], v[222:225], v[108:111]
	v_mfma_f32_16x16x32_f16 v[100:103], v[178:181], v[222:225], v[100:103]
	v_mfma_f32_16x16x32_f16 v[100:103], v[174:177], v[214:217], v[100:103]
	v_mfma_f32_16x16x32_f16 v[84:87], v[174:177], v[218:221], v[84:87]
	v_mfma_f32_16x16x32_f16 v[84:87], v[178:181], v[226:229], v[84:87]
	v_mfma_f32_16x16x32_f16 v[92:95], v[170:173], v[226:229], v[92:95]
	v_mfma_f32_16x16x32_f16 v[92:95], v[166:169], v[218:221], v[92:95]
	s_setprio 0
	s_setprio 1
	v_mfma_f32_16x16x32_f16 v[104:107], v[182:185], v[198:201], v[104:107]
	v_mfma_f32_16x16x32_f16 v[104:107], v[186:189], v[206:209], v[104:107]
	v_mfma_f32_16x16x32_f16 v[96:99], v[194:197], v[206:209], v[96:99]
	v_mfma_f32_16x16x32_f16 v[96:99], v[190:193], v[198:201], v[96:99]
	v_mfma_f32_16x16x32_f16 v[80:83], v[190:193], v[202:205], v[80:83]
	v_mfma_f32_16x16x32_f16 v[80:83], v[194:197], v[210:213], v[80:83]
	v_mfma_f32_16x16x32_f16 v[88:91], v[186:189], v[210:213], v[88:91]
	v_mfma_f32_16x16x32_f16 v[88:91], v[182:185], v[202:205], v[88:91]
	v_mfma_f32_16x16x32_f16 v[76:79], v[182:185], v[214:217], v[76:79]
	v_mfma_f32_16x16x32_f16 v[76:79], v[186:189], v[222:225], v[76:79]
	v_mfma_f32_16x16x32_f16 v[72:75], v[194:197], v[222:225], v[72:75]
	v_mfma_f32_16x16x32_f16 v[72:75], v[190:193], v[214:217], v[72:75]
	v_mfma_f32_16x16x32_f16 v[64:67], v[190:193], v[218:221], v[64:67]
	v_mfma_f32_16x16x32_f16 v[64:67], v[194:197], v[226:229], v[64:67]
	v_mfma_f32_16x16x32_f16 v[68:71], v[186:189], v[226:229], v[68:71]
	v_mfma_f32_16x16x32_f16 v[68:71], v[182:185], v[218:221], v[68:71]
	s_setprio 0
	s_barrier
	s_add_i32 s34, s46, s36
	v_lshl_add_u64 v[138:139], v[138:139], 0, s[14:15]
	s_mov_b32 m0, s34
	ds_read_b128 v[198:201], v155 offset:49152
	ds_read_b128 v[202:205], v155 offset:51200
	ds_read_b128 v[206:209], v156 offset:49152
	ds_read_b128 v[210:213], v156 offset:51200
	ds_read_b128 v[214:217], v155 offset:53248
	ds_read_b128 v[218:221], v155 offset:55296
	ds_read_b128 v[222:225], v156 offset:53248
	ds_read_b128 v[226:229], v156 offset:55296
	global_load_lds_dwordx4 v[138:139], off
	s_add_i32 m0, s34, 0x2000
	s_add_u32 s30, s30, 0x380080
	v_lshl_add_u64 v[138:139], v[144:145], 0, s[14:15]
	s_addc_u32 s31, s31, 0
	s_add_i32 s34, s47, s36
	global_load_lds_dwordx4 v[138:139], off
	v_lshl_add_u64 v[138:139], s[30:31], 0, v[128:129]
	s_mov_b32 m0, s34
	s_nop 0
	global_load_lds_dwordx4 v[138:139], off
	v_lshl_add_u64 v[138:139], s[30:31], 0, v[130:131]
	s_add_i32 m0, s34, 0x2000
	s_nop 0
	global_load_lds_dwordx4 v[138:139], off
	v_lshl_add_u64 v[138:139], v[230:231], 0, s[14:15]
	s_mov_b32 m0, s41
	s_nop 0
	global_load_lds_dwordx4 v[138:139], off
	v_lshl_add_u64 v[138:139], v[232:233], 0, s[14:15]
	s_mov_b32 m0, s42
	s_nop 0
	global_load_lds_dwordx4 v[138:139], off
	s_waitcnt vmcnt(8)
	s_waitcnt lgkmcnt(0)
	s_barrier
	s_setprio 1
	s_waitcnt lgkmcnt(0)
	v_mfma_f32_16x16x32_f16 v[60:63], v[166:169], v[198:201], v[60:63]
	v_mfma_f32_16x16x32_f16 v[60:63], v[170:173], v[206:209], v[60:63]
	v_mfma_f32_16x16x32_f16 v[56:59], v[178:181], v[206:209], v[56:59]
	v_mfma_f32_16x16x32_f16 v[56:59], v[174:177], v[198:201], v[56:59]
	v_mfma_f32_16x16x32_f16 v[48:51], v[174:177], v[202:205], v[48:51]
	v_mfma_f32_16x16x32_f16 v[48:51], v[178:181], v[210:213], v[48:51]
	v_mfma_f32_16x16x32_f16 v[52:55], v[170:173], v[210:213], v[52:55]
	v_mfma_f32_16x16x32_f16 v[52:55], v[166:169], v[202:205], v[52:55]
	v_mfma_f32_16x16x32_f16 v[40:43], v[166:169], v[214:217], v[40:43]
	v_mfma_f32_16x16x32_f16 v[40:43], v[170:173], v[222:225], v[40:43]
	v_mfma_f32_16x16x32_f16 v[32:35], v[178:181], v[222:225], v[32:35]
	v_mfma_f32_16x16x32_f16 v[32:35], v[174:177], v[214:217], v[32:35]
	v_mfma_f32_16x16x32_f16 v[8:11], v[174:177], v[218:221], v[8:11]
	v_mfma_f32_16x16x32_f16 v[8:11], v[178:181], v[226:229], v[8:11]
	v_mfma_f32_16x16x32_f16 v[12:15], v[170:173], v[226:229], v[12:15]
	v_mfma_f32_16x16x32_f16 v[12:15], v[166:169], v[218:221], v[12:15]
	s_setprio 0
	s_setprio 1
	v_mfma_f32_16x16x32_f16 v[44:47], v[182:185], v[198:201], v[44:47]
	v_mfma_f32_16x16x32_f16 v[44:47], v[186:189], v[206:209], v[44:47]
	v_mfma_f32_16x16x32_f16 v[36:39], v[194:197], v[206:209], v[36:39]
	v_mfma_f32_16x16x32_f16 v[36:39], v[190:193], v[198:201], v[36:39]
	v_mfma_f32_16x16x32_f16 v[24:27], v[190:193], v[202:205], v[24:27]
	v_mfma_f32_16x16x32_f16 v[24:27], v[194:197], v[210:213], v[24:27]
	v_mfma_f32_16x16x32_f16 v[28:31], v[186:189], v[210:213], v[28:31]
	v_mfma_f32_16x16x32_f16 v[28:31], v[182:185], v[202:205], v[28:31]
	v_mfma_f32_16x16x32_f16 v[20:23], v[182:185], v[214:217], v[20:23]
	v_mfma_f32_16x16x32_f16 v[20:23], v[186:189], v[222:225], v[20:23]
	v_mfma_f32_16x16x32_f16 v[16:19], v[194:197], v[222:225], v[16:19]
	v_mfma_f32_16x16x32_f16 v[16:19], v[190:193], v[214:217], v[16:19]
	v_mfma_f32_16x16x32_f16 v[0:3], v[190:193], v[218:221], v[0:3]
	v_mfma_f32_16x16x32_f16 v[0:3], v[194:197], v[226:229], v[0:3]
	v_mfma_f32_16x16x32_f16 v[4:7], v[186:189], v[226:229], v[4:7]
	v_mfma_f32_16x16x32_f16 v[4:7], v[182:185], v[218:221], v[4:7]
	s_setprio 0
	s_barrier
	s_add_i32 s58, s58, 2
	s_add_u32 s56, s56, 0x100
	s_addc_u32 s57, s57, 0
	s_add_u32 s28, s28, 0x100
	s_addc_u32 s29, s29, 0
	s_cmpk_gt_u32 s58, 0xdd
	s_cbranch_scc0 .LBB2_20
	v_lshl_add_u32 v144, s55, 8, v137
	v_ashrrev_i32_e32 v145, 31, v144
	v_lshl_add_u64 v[138:139], v[144:145], 2, s[10:11]
	global_load_dword v136, v[138:139], off
	global_load_dword v140, v[138:139], off offset:64
	global_load_dword v142, v[138:139], off offset:128
	global_load_dword v146, v[138:139], off offset:192
	global_load_dword v148, v[138:139], off offset:512
	global_load_dword v174, v[138:139], off offset:576
	global_load_dword v176, v[138:139], off offset:640
	s_nop 0
	global_load_dword v138, v[138:139], off offset:704
	v_lshl_or_b32 v166, s54, 8, v141
	v_ashrrev_i32_e32 v167, 31, v166
	v_or_b32_e32 v168, 16, v144
	v_or_b32_e32 v170, 32, v144
	v_or_b32_e32 v172, 48, v144
	v_lshl_add_u64 v[166:167], v[166:167], 2, s[8:9]
	v_lshlrev_b64 v[144:145], 14, v[144:145]
	v_ashrrev_i32_e32 v169, 31, v168
	v_ashrrev_i32_e32 v171, 31, v170
	v_ashrrev_i32_e32 v173, 31, v172
	v_lshl_add_u64 v[144:145], v[166:167], 0, v[144:145]
	v_lshlrev_b64 v[168:169], 14, v[168:169]
	v_lshlrev_b64 v[170:171], 14, v[170:171]
	v_lshlrev_b64 v[172:173], 14, v[172:173]
	v_add_co_u32_e32 v178, vcc, s48, v144
	v_lshl_add_u64 v[168:169], v[166:167], 0, v[168:169]
	v_lshl_add_u64 v[170:171], v[166:167], 0, v[170:171]
	v_lshl_add_u64 v[166:167], v[166:167], 0, v[172:173]
	v_lshl_add_u64 v[172:173], v[144:145], 0, s[16:17]
	v_addc_co_u32_e32 v179, vcc, 0, v145, vcc
	s_mov_b32 s55, s45
	s_mov_b32 s54, s53
	s_mov_b64 s[28:29], s[26:27]
	s_mov_b64 s[30:31], s[24:25]
	s_waitcnt vmcnt(0)
	v_pk_mul_f32 v[126:127], v[136:137], v[126:127] op_sel_hi:[0,1]
	v_pk_mul_f32 v[124:125], v[136:137], v[124:125] op_sel_hi:[0,1]
	v_pk_mul_f32 v[122:123], v[136:137], v[122:123] op_sel_hi:[0,1]
	v_pk_mul_f32 v[120:121], v[136:137], v[120:121] op_sel_hi:[0,1]
	v_pk_mul_f32 v[46:47], v[148:149], v[46:47] op_sel_hi:[0,1]
	v_pk_mul_f32 v[44:45], v[148:149], v[44:45] op_sel_hi:[0,1]
	v_pk_mul_f32 v[106:107], v[136:137], v[106:107] op_sel_hi:[0,1]
	v_pk_mul_f32 v[104:105], v[136:137], v[104:105] op_sel_hi:[0,1]
	v_pk_mul_f32 v[98:99], v[136:137], v[98:99] op_sel_hi:[0,1]
	v_pk_mul_f32 v[96:97], v[136:137], v[96:97] op_sel_hi:[0,1]
	v_pk_mul_f32 v[118:119], v[140:141], v[118:119] op_sel_hi:[0,1]
	v_pk_mul_f32 v[116:117], v[140:141], v[116:117] op_sel_hi:[0,1]
	v_pk_mul_f32 v[114:115], v[140:141], v[114:115] op_sel_hi:[0,1]
	v_pk_mul_f32 v[112:113], v[140:141], v[112:113] op_sel_hi:[0,1]
	v_pk_mul_f32 v[90:91], v[140:141], v[90:91] op_sel_hi:[0,1]
	v_pk_mul_f32 v[88:89], v[140:141], v[88:89] op_sel_hi:[0,1]
	v_pk_mul_f32 v[82:83], v[140:141], v[82:83] op_sel_hi:[0,1]
	v_pk_mul_f32 v[80:81], v[140:141], v[80:81] op_sel_hi:[0,1]
	v_pk_mul_f32 v[110:111], v[142:143], v[110:111] op_sel_hi:[0,1]
	v_pk_mul_f32 v[108:109], v[142:143], v[108:109] op_sel_hi:[0,1]
	v_pk_mul_f32 v[102:103], v[142:143], v[102:103] op_sel_hi:[0,1]
	v_pk_mul_f32 v[100:101], v[142:143], v[100:101] op_sel_hi:[0,1]
	v_pk_mul_f32 v[78:79], v[142:143], v[78:79] op_sel_hi:[0,1]
	v_pk_mul_f32 v[76:77], v[142:143], v[76:77] op_sel_hi:[0,1]
	v_pk_mul_f32 v[74:75], v[142:143], v[74:75] op_sel_hi:[0,1]
	v_pk_mul_f32 v[72:73], v[142:143], v[72:73] op_sel_hi:[0,1]
	v_pk_mul_f32 v[94:95], v[146:147], v[94:95] op_sel_hi:[0,1]
	v_pk_mul_f32 v[92:93], v[146:147], v[92:93] op_sel_hi:[0,1]
	v_pk_mul_f32 v[86:87], v[146:147], v[86:87] op_sel_hi:[0,1]
	v_pk_mul_f32 v[84:85], v[146:147], v[84:85] op_sel_hi:[0,1]
	v_pk_mul_f32 v[70:71], v[146:147], v[70:71] op_sel_hi:[0,1]
	v_pk_mul_f32 v[68:69], v[146:147], v[68:69] op_sel_hi:[0,1]
	v_pk_mul_f32 v[66:67], v[146:147], v[66:67] op_sel_hi:[0,1]
	v_pk_mul_f32 v[64:65], v[146:147], v[64:65] op_sel_hi:[0,1]
	v_pk_mul_f32 v[62:63], v[148:149], v[62:63] op_sel_hi:[0,1]
	v_pk_mul_f32 v[60:61], v[148:149], v[60:61] op_sel_hi:[0,1]
	global_store_dwordx4 v[144:145], v[124:127], off
	global_store_dwordx4 v[144:145], v[120:123], off offset:64
	global_store_dwordx4 v[144:145], v[104:107], off offset:512
	global_store_dwordx4 v[144:145], v[96:99], off offset:576
	global_store_dwordx4 v[168:169], v[116:119], off
	global_store_dwordx4 v[168:169], v[112:115], off offset:64
	global_store_dwordx4 v[168:169], v[88:91], off offset:512
	global_store_dwordx4 v[168:169], v[80:83], off offset:576
	global_store_dwordx4 v[170:171], v[108:111], off
	global_store_dwordx4 v[170:171], v[100:103], off offset:64
	global_store_dwordx4 v[170:171], v[76:79], off offset:512
	global_store_dwordx4 v[170:171], v[72:75], off offset:576
	global_store_dwordx4 v[166:167], v[92:95], off
	global_store_dwordx4 v[166:167], v[84:87], off offset:64
	global_store_dwordx4 v[166:167], v[68:71], off offset:512
	global_store_dwordx4 v[166:167], v[64:67], off offset:576
	global_store_dwordx4 v[178:179], v[60:63], off
	global_store_dwordx4 v[172:173], v[44:47], off offset:512
	v_pk_mul_f32 v[30:31], v[174:175], v[30:31] op_sel_hi:[0,1]
	v_pk_mul_f32 v[28:29], v[174:175], v[28:29] op_sel_hi:[0,1]
	v_add_co_u32_e32 v46, vcc, s49, v144
	v_lshl_add_u64 v[44:45], v[144:145], 0, s[18:19]
	s_nop 0
	v_addc_co_u32_e32 v47, vcc, 0, v145, vcc
	global_store_dwordx4 v[44:45], v[28:31], off offset:512
	v_pk_mul_f32 v[18:19], v[176:177], v[18:19] op_sel_hi:[0,1]
	v_pk_mul_f32 v[16:17], v[176:177], v[16:17] op_sel_hi:[0,1]
	v_add_co_u32_e32 v30, vcc, s50, v144
	v_lshl_add_u64 v[28:29], v[144:145], 0, s[20:21]
	s_nop 0
	v_addc_co_u32_e32 v31, vcc, 0, v145, vcc
	v_pk_mul_f32 v[38:39], v[148:149], v[38:39] op_sel_hi:[0,1]
	v_pk_mul_f32 v[36:37], v[148:149], v[36:37] op_sel_hi:[0,1]
	v_pk_mul_f32 v[26:27], v[174:175], v[26:27] op_sel_hi:[0,1]
	v_pk_mul_f32 v[24:25], v[174:175], v[24:25] op_sel_hi:[0,1]
	global_store_dwordx4 v[28:29], v[16:19], off offset:576
	global_store_dwordx4 v[172:173], v[36:39], off offset:576
	global_store_dwordx4 v[44:45], v[24:27], off offset:576
	v_add_co_u32_e32 v18, vcc, s51, v144
	v_pk_mul_f32 v[38:39], v[174:175], v[54:55] op_sel_hi:[0,1]
	v_pk_mul_f32 v[36:37], v[174:175], v[52:53] op_sel_hi:[0,1]
	v_pk_mul_f32 v[26:27], v[176:177], v[42:43] op_sel_hi:[0,1]
	v_pk_mul_f32 v[24:25], v[176:177], v[40:41] op_sel_hi:[0,1]
	v_addc_co_u32_e32 v19, vcc, 0, v145, vcc
	v_pk_mul_f32 v[58:59], v[148:149], v[58:59] op_sel_hi:[0,1]
	v_pk_mul_f32 v[56:57], v[148:149], v[56:57] op_sel_hi:[0,1]
	global_store_dwordx4 v[46:47], v[36:39], off
	global_store_dwordx4 v[30:31], v[24:27], off
	v_pk_mul_f32 v[22:23], v[176:177], v[22:23] op_sel_hi:[0,1]
	v_pk_mul_f32 v[38:39], v[174:175], v[50:51] op_sel_hi:[0,1]
	v_pk_mul_f32 v[36:37], v[174:175], v[48:49] op_sel_hi:[0,1]
	v_pk_mul_f32 v[26:27], v[176:177], v[34:35] op_sel_hi:[0,1]
	v_pk_mul_f32 v[24:25], v[176:177], v[32:33] op_sel_hi:[0,1]
	v_pk_mul_f32 v[20:21], v[176:177], v[20:21] op_sel_hi:[0,1]
	v_lshl_add_u64 v[16:17], v[144:145], 0, s[22:23]
	v_pk_mul_f32 v[14:15], v[138:139], v[14:15] op_sel_hi:[0,1]
	v_pk_mul_f32 v[12:13], v[138:139], v[12:13] op_sel_hi:[0,1]
	v_pk_mul_f32 v[10:11], v[138:139], v[10:11] op_sel_hi:[0,1]
	v_pk_mul_f32 v[8:9], v[138:139], v[8:9] op_sel_hi:[0,1]
	v_pk_mul_f32 v[6:7], v[138:139], v[6:7] op_sel_hi:[0,1]
	v_pk_mul_f32 v[4:5], v[138:139], v[4:5] op_sel_hi:[0,1]
	v_pk_mul_f32 v[2:3], v[138:139], v[2:3] op_sel_hi:[0,1]
	v_pk_mul_f32 v[0:1], v[138:139], v[0:1] op_sel_hi:[0,1]
	s_mov_b64 vcc, s[0:1]
	global_store_dwordx4 v[172:173], v[56:59], off offset:64
	global_store_dwordx4 v[44:45], v[36:39], off offset:64
	global_store_dwordx4 v[28:29], v[24:27], off offset:64
	global_store_dwordx4 v[28:29], v[20:23], off offset:512
	global_store_dwordx4 v[18:19], v[12:15], off
	global_store_dwordx4 v[16:17], v[8:11], off offset:64
	global_store_dwordx4 v[16:17], v[4:7], off offset:512
	global_store_dwordx4 v[16:17], v[0:3], off offset:576
	s_cbranch_vccz .LBB2_8
	s_waitcnt vmcnt(0)
	s_cmpk_gt_u32 s33, 0xff
	s_cbranch_scc1 .LBB2_24
	s_barrier
